# L1: waves 8-15 start staggered by s_sleep 64 after the barrier
# speedup vs baseline: 1.0038x; 1.0031x over previous
.LBB4_14:
	v_lshrrev_b32_e32 v2, 3, v0
	s_load_dwordx2 s[4:5], s[0:1], 0x40
	v_and_b32_e32 v2, 0x78, v2
	s_movk_i32 s2, 0x90
	v_and_b32_e32 v97, 7, v0
	s_sub_i32 s0, s18, s8
	v_and_b32_e32 v1, 63, v0
	v_mov_b32_e32 v89, 0
	v_mad_u32_u24 v3, v2, s2, 0
	v_bfe_u32 v96, v0, 3, 3
	v_and_b32_e32 v99, 15, v0
	v_bfe_u32 v4, v0, 4, 2
	s_add_i32 s0, s0, 7
	v_mul_u32_u24_e32 v5, 0x90, v97
	v_and_b32_e32 v0, 48, v0
	s_ashr_i32 s9, s0, 3
	v_cmp_eq_u32_e64 s[0:1], 0, v1
	v_mad_u32_u24 v1, v96, s2, v3
	v_lshlrev_b32_e32 v2, 3, v4
	v_add3_u32 v103, v3, v5, v0
	v_mov_b32_e32 v3, v89
	v_lshlrev_b32_e32 v98, 4, v97
	v_add_u32_e32 v0, 0, v0
	v_lshlrev_b32_e32 v88, 2, v4
	v_lshl_add_u64 v[90:91], s[22:23], 0, v[2:3]
	v_mul_u32_u24_e32 v2, 0x210, v99
	v_or_b32_e32 v100, 8, v97
	v_or_b32_e32 v101, 16, v97
	v_add_u32_e32 v102, 0, v98
	v_cmp_gt_u32_e64 s[2:3], 8, v99
	s_waitcnt lgkmcnt(0)
	v_lshl_add_u64 v[92:93], s[4:5], 0, v[88:89]
	v_lshlrev_b32_e32 v88, 2, v88
	v_add_u32_e32 v104, v1, v98
	v_add_u32_e32 v105, v0, v2
	s_lshl_b32 s19, s36, 3
	s_add_i32 s19, s19, s8
	v_add_u32_e32 v94, s19, v96
	v_cmp_gt_i32_e64 s[4:5], s18, v94
	v_mov_b32_e32 v32, 0
	v_mov_b32_e32 v33, 0
	v_mov_b32_e32 v34, 0
	v_mov_b32_e32 v35, 0
	s_and_saveexec_b64 s[6:7], s[4:5]
	v_lshl_add_u32 v36, v94, 1, v94
	v_lshlrev_b32_e32 v36, 2, v36
	global_load_dwordx4 v[32:35], v36, s[10:11]
	s_mov_b64 exec, s[6:7]
	s_waitcnt vmcnt(6)
	ds_write_b128 v40, v[6:9]
	s_waitcnt vmcnt(5)
	ds_write_b128 v40, v[10:13] offset:16896
	s_waitcnt vmcnt(4)
	ds_write_b128 v41, v[14:17]
	s_waitcnt vmcnt(3)
	ds_write_b128 v41, v[18:21] offset:16384
	s_waitcnt vmcnt(2)
	ds_write_b128 v41, v[22:25] offset:32768
	s_waitcnt vmcnt(1)
	ds_write_b128 v41, v[26:29] offset:49152
	s_and_saveexec_b64 s[6:7], s[34:35]
	ds_write_b128 v38, v[42:45]
	s_mov_b64 exec, s[6:7]
	s_waitcnt vmcnt(0)
	v_sub_u32_e32 v72, v33, v32
	v_sub_u32_e32 v108, v34, v33
	v_sub_u32_e32 v35, v35, v34
	v_add_lshl_u32 v37, v32, v97, 2
	v_add_lshl_u32 v38, v33, v97, 2
	v_add_lshl_u32 v39, v34, v97, 2
	v_mov_b32_e32 v36, 0x4000000
	v_mov_b32_e32 v68, 0x4000000
	v_mov_b32_e32 v74, 0x4000000
	v_mov_b32_e32 v85, 0x4000000
	v_mov_b32_e32 v84, 0x4000000
	v_mov_b32_e32 v109, 0x4000000
	v_mov_b32_e32 v107, 0x4000000
	v_mov_b32_e32 v106, 0x4000000
	v_mov_b32_e32 v95, 0x4000000
	s_mov_b64 s[6:7], exec
	v_cmp_lt_i32_e32 vcc, v97, v72
	s_and_b64 exec, exec, vcc
	global_load_dword v36, v37, s[12:13]
	v_cmp_lt_i32_e32 vcc, v100, v72
	s_and_b64 exec, exec, vcc
	global_load_dword v68, v37, s[12:13] offset:32
	v_cmp_lt_i32_e32 vcc, v101, v72
	s_and_b64 exec, exec, vcc
	global_load_dword v74, v37, s[12:13] offset:64
	s_mov_b64 exec, s[6:7]
	v_cmp_lt_i32_e32 vcc, v97, v108
	s_and_b64 exec, exec, vcc
	global_load_dword v85, v38, s[12:13]
	v_cmp_lt_i32_e32 vcc, v100, v108
	s_and_b64 exec, exec, vcc
	global_load_dword v84, v38, s[12:13] offset:32
	v_cmp_lt_i32_e32 vcc, v101, v108
	s_and_b64 exec, exec, vcc
	global_load_dword v109, v38, s[12:13] offset:64
	s_mov_b64 exec, s[6:7]
	v_cmp_lt_i32_e32 vcc, v97, v35
	s_and_b64 exec, exec, vcc
	global_load_dword v107, v39, s[12:13]
	v_cmp_lt_i32_e32 vcc, v100, v35
	s_and_b64 exec, exec, vcc
	global_load_dword v106, v39, s[12:13] offset:32
	v_cmp_lt_i32_e32 vcc, v101, v35
	s_and_b64 exec, exec, vcc
	global_load_dword v95, v39, s[12:13] offset:64
	s_mov_b64 exec, s[6:7]
	s_waitcnt lgkmcnt(0)
	s_barrier
	s_cmp_ge_i32 s36, s9
	s_cbranch_scc1 .LBB4_103
	s_cmp_lt_u32 s36, 8
	s_cbranch_scc1 .Lp1_nostagger
	s_sleep 64
